# speedup vs baseline: 1.0680x; 1.0286x over previous
.LBB1_2:
	s_or_b64 exec, exec, s[8:9]
	s_ashr_i32 s9, s2, 3
	s_and_b32 s8, s2, 7
	s_and_b32 s9, s9, -8
	s_bfe_u32 s20, s3, 0x20006
	s_or_b32 s10, s9, s8
	s_lshl_b32 s2, s2, 4
	s_lshr_b32 s22, s3, 6
	v_bfe_u32 v1, v0, 5, 1
	s_and_b32 s2, s2, 0x380
	s_lshl_b32 s8, s20, 5
	s_ashr_i32 s11, s10, 31
	s_or_b32 s2, s8, s2
	s_lshl_b64 s[8:9], s[10:11], 19
	v_lshl_or_b32 v2, s22, 1, v1
	s_waitcnt lgkmcnt(0)
	s_add_u32 s14, s4, s8
	v_lshlrev_b32_e32 v6, 9, v2
	v_lshlrev_b32_e32 v2, 2, v2
	v_and_b32_e32 v5, 31, v0
	s_addc_u32 s15, s5, s9
	v_and_b32_e32 v2, 12, v2
	s_bfe_u32 s4, s3, 0x20007
	v_bitop3_b32 v2, v2, v5, s4 bitop3:0x36
	s_lshl_b32 s4, s22, 10
	v_lshl_or_b32 v192, v2, 4, v6
	s_add_i32 s21, s4, 0
	s_mov_b32 s4, m0
	s_mov_b32 m0, s21
	s_nop 0
	global_load_lds_dwordx4 v192, s[6:7]
	s_mov_b32 m0, s4
	s_add_u32 s4, s6, 0x2000
	s_addc_u32 s5, s7, 0
	s_add_i32 s31, s21, 0x2000
	s_mov_b32 s8, m0
	s_mov_b32 m0, s31
	s_nop 0
	global_load_lds_dwordx4 v192, s[4:5]
	s_mov_b32 m0, s8
	s_add_u32 s4, s6, 0x4000
	s_addc_u32 s5, s7, 0
	s_add_i32 s33, s21, 0x4000
	s_mov_b32 s8, m0
	s_mov_b32 m0, s33
	s_nop 0
	global_load_lds_dwordx4 v192, s[4:5]
	s_mov_b32 m0, s8
	s_add_u32 s4, s6, 0x6000
	s_addc_u32 s5, s7, 0
	s_add_i32 s34, s21, 0x6000
	s_mov_b32 s8, m0
	s_mov_b32 m0, s34
	s_nop 0
	global_load_lds_dwordx4 v192, s[4:5]
	s_mov_b32 m0, s8
	s_add_u32 s4, s6, 0x8000
	s_addc_u32 s5, s7, 0
	s_add_i32 s23, s21, 0x8000
	s_mov_b32 s8, m0
	s_mov_b32 m0, s23
	s_nop 0
	global_load_lds_dwordx4 v192, s[4:5]
	s_mov_b32 m0, s8
	s_add_u32 s4, s6, 0xa000
	s_addc_u32 s5, s7, 0
	s_add_i32 s24, s21, 0xa000
	s_mov_b32 s8, m0
	s_mov_b32 m0, s24
	s_nop 0
	global_load_lds_dwordx4 v192, s[4:5]
	s_mov_b32 m0, s8
	s_add_u32 s4, s6, 0xc000
	s_addc_u32 s5, s7, 0
	s_add_i32 s25, s21, 0xc000
	s_mov_b32 s8, m0
	s_mov_b32 m0, s25
	s_nop 0
	global_load_lds_dwordx4 v192, s[4:5]
	s_mov_b32 m0, s8
	s_add_u32 s4, s6, 0xe000
	s_addc_u32 s5, s7, 0
	s_add_i32 s26, s21, 0xe000
	s_mov_b32 s8, m0
	s_mov_b32 m0, s26
	s_nop 0
	global_load_lds_dwordx4 v192, s[4:5]
	s_mov_b32 m0, s8
	s_and_b32 s4, s2, 0x380
	s_lshl_b32 s4, s4, 9
	s_add_u32 s4, s14, s4
	s_addc_u32 s5, s15, 0
	s_add_i32 s27, s21, 0x10000
	s_add_i32 s28, s21, 0x12000
	s_add_i32 s29, s21, 0x14000
	s_add_i32 s30, s21, 0x16000
	s_mov_b32 s8, m0
	s_mov_b32 m0, s27
	s_nop 0
	global_load_lds_dwordx4 v192, s[4:5]
	s_mov_b32 m0, s8
	s_add_u32 s40, s4, 0x2000
	s_addc_u32 s41, s5, 0
	s_mov_b32 s8, m0
	s_mov_b32 m0, s28
	s_nop 0
	global_load_lds_dwordx4 v192, s[40:41]
	s_mov_b32 m0, s8
	s_add_u32 s40, s4, 0x4000
	s_addc_u32 s41, s5, 0
	s_mov_b32 s8, m0
	s_mov_b32 m0, s29
	s_nop 0
	global_load_lds_dwordx4 v192, s[40:41]
	s_mov_b32 m0, s8
	s_add_u32 s40, s4, 0x6000
	s_addc_u32 s41, s5, 0
	s_mov_b32 s8, m0
	s_mov_b32 m0, s30
	s_nop 0
	global_load_lds_dwordx4 v192, s[40:41]
	s_mov_b32 m0, s8
	s_add_u32 s40, s4, 0x8000
	s_addc_u32 s41, s5, 0
	s_add_i32 s42, s21, 0x18000
	s_mov_b32 s8, m0
	s_mov_b32 m0, s42
	s_nop 0
	global_load_lds_dwordx4 v192, s[40:41]
	s_mov_b32 m0, s8
	s_add_u32 s40, s4, 0xa000
	s_addc_u32 s41, s5, 0
	s_add_i32 s42, s21, 0x1a000
	s_mov_b32 s8, m0
	s_mov_b32 m0, s42
	s_nop 0
	global_load_lds_dwordx4 v192, s[40:41]
	s_mov_b32 m0, s8
	s_add_u32 s40, s4, 0xc000
	s_addc_u32 s41, s5, 0
	s_add_i32 s42, s21, 0x1c000
	s_mov_b32 s8, m0
	s_mov_b32 m0, s42
	s_nop 0
	global_load_lds_dwordx4 v192, s[40:41]
	s_mov_b32 m0, s8
	s_add_u32 s40, s4, 0xe000
	s_addc_u32 s41, s5, 0
	s_add_i32 s42, s21, 0x1e000
	s_mov_b32 s8, m0
	s_mov_b32 m0, s42
	s_nop 0
	global_load_lds_dwordx4 v192, s[40:41]
	s_mov_b32 m0, s8
	s_movk_i32 s4, 0xff
	v_cmp_lt_u32_e32 vcc, s4, v0
	s_and_saveexec_b64 s[4:5], vcc
	s_xor_b64 s[4:5], exec, s[4:5]
	s_cbranch_execz .LBB1_4
	s_load_dwordx2 s[8:9], s[0:1], 0x20
	v_add_u32_e32 v2, 0xffffff00, v0
	v_mov_b32_e32 v3, 0
	s_waitcnt lgkmcnt(0)
	v_lshl_add_u64 v[6:7], v[2:3], 2, s[8:9]
	global_load_dword v3, v[6:7], off
	v_lshl_add_u32 v2, v2, 2, 0
	v_add_u32_e32 v2, 0x22400, v2
	s_waitcnt vmcnt(0)
	ds_write_b32 v2, v3

.LBB1_6:
	s_or_b64 exec, exec, s[4:5]
	s_lshr_b32 s5, s3, 8
	s_lshl_b32 s16, s20, 12
	s_lshl_b32 s4, s5, 5
	s_add_i32 s35, s16, 0
	s_add_u32 s18, s6, 0x18000
	v_and_b32_e32 v2, 12, v2
	v_bfe_u32 v0, v0, 2, 2
	s_addc_u32 s19, s7, 0
	v_bitop3_b32 v0, v2, v1, v0 bitop3:0x36
	s_add_u32 s16, s14, 0x8000
	v_lshlrev_b32_e32 v100, 4, v0
	v_or_b32_e32 v0, s4, v5
	s_addc_u32 s17, s15, 0
	s_lshl_b32 s36, s5, 7
	v_lshl_add_u32 v101, v0, 9, 0
	v_lshl_or_b32 v0, v1, 4, s36
	v_add_u32_e32 v0, 0, v0
	v_add_u32_e32 v83, v101, v100
	s_waitcnt vmcnt(0)
	s_waitcnt lgkmcnt(0)
	s_barrier
	s_lshl_b32 s40, s20, 14
	s_add_i32 s40, s40, 0x10000
	v_lshl_add_u32 v108, v5, 9, s40
	v_add_u32_e32 v109, v108, v100
	ds_read_b128 v[68:71], v109
	ds_read_b128 v[76:79], v109 offset:256
	v_xor_b32_e32 v109, 0x20, v100
	v_add_u32_e32 v109, v108, v109
	ds_read_b128 v[60:63], v109
	ds_read_b128 v[72:75], v109 offset:256
	v_xor_b32_e32 v109, 0x40, v100
	v_add_u32_e32 v109, v108, v109
	ds_read_b128 v[52:55], v109
	ds_read_b128 v[64:67], v109 offset:256
	v_xor_b32_e32 v109, 0x60, v100
	v_add_u32_e32 v109, v108, v109
	ds_read_b128 v[48:51], v109
	ds_read_b128 v[56:59], v109 offset:256
	v_xor_b32_e32 v109, 0x80, v100
	v_add_u32_e32 v109, v108, v109
	ds_read_b128 v[36:39], v109
	ds_read_b128 v[44:47], v109 offset:256
	v_xor_b32_e32 v109, 0xa0, v100
	v_add_u32_e32 v109, v108, v109
	ds_read_b128 v[28:31], v109
	ds_read_b128 v[40:43], v109 offset:256
	v_xor_b32_e32 v109, 0xc0, v100
	v_add_u32_e32 v109, v108, v109
	ds_read_b128 v[24:27], v109
	ds_read_b128 v[32:35], v109 offset:256
	v_xor_b32_e32 v109, 0xe0, v100
	v_add_u32_e32 v109, v108, v109
	ds_read_b128 v[20:23], v109
	ds_read_b128 v[16:19], v109 offset:256
	s_waitcnt lgkmcnt(0)
	s_barrier
	s_add_u32 s40, s6, 0x10000
	s_addc_u32 s41, s7, 0
	s_mov_b32 s42, m0
	s_mov_b32 m0, s27
	s_nop 0
	global_load_lds_dwordx4 v192, s[40:41]
	s_mov_b32 m0, s42
	s_add_u32 s40, s6, 0x12000
	s_addc_u32 s41, s7, 0
	s_mov_b32 s42, m0
	s_mov_b32 m0, s28
	s_nop 0
	global_load_lds_dwordx4 v192, s[40:41]
	s_mov_b32 m0, s42
	s_add_u32 s40, s6, 0x14000
	s_addc_u32 s41, s7, 0
	s_mov_b32 s42, m0
	s_mov_b32 m0, s29
	s_nop 0
	global_load_lds_dwordx4 v192, s[40:41]
	s_mov_b32 m0, s42
	s_add_u32 s40, s6, 0x16000
	s_addc_u32 s41, s7, 0
	s_mov_b32 s42, m0
	s_mov_b32 m0, s30
	s_nop 0
	global_load_lds_dwordx4 v192, s[40:41]
	s_mov_b32 m0, s42
	v_add_u32_e32 v80, 0x22000, v0
	ds_read_b128 v[84:87], v83
	ds_read_b128 v[0:3], v80
	ds_read_b128 v[4:7], v80 offset:32
	ds_read_b128 v[8:11], v80 offset:64
	ds_read_b128 v[12:15], v80 offset:96
	ds_read_b128 v[88:91], v83 offset:256
	s_waitcnt vmcnt(15) lgkmcnt(1)
	v_mfma_f32_32x32x16_bf16 v[0:15], v[84:87], v[68:71], v[0:15]
	v_xor_b32_e32 v102, 32, v100
	v_add_u32_e32 v84, v101, v102
	v_xor_b32_e32 v103, 64, v100
	v_add_u32_e32 v85, v101, v103
	v_xor_b32_e32 v104, 0x60, v100
	v_xor_b32_e32 v105, 0x80, v100
	v_xor_b32_e32 v106, 0xa0, v100
	s_waitcnt vmcnt(7) lgkmcnt(0)
	v_mfma_f32_32x32x16_bf16 v[0:15], v[88:91], v[76:79], v[0:15]
	ds_read_b128 v[86:89], v84
	ds_read_b128 v[90:93], v84 offset:256
	v_xor_b32_e32 v107, 0xe0, v100
	v_lshl_add_u32 v81, v81, 4, s35
	v_add_u32_e32 v81, 0x18000, v81
	v_lshl_add_u32 v82, s5, 11, v81
	s_add_u32 s36, s6, 0x1a000
	s_addc_u32 s37, s7, 0
	s_waitcnt lgkmcnt(1)
	v_mfma_f32_32x32x16_bf16 v[0:15], v[86:89], v[60:63], v[0:15]
	s_add_u32 s38, s6, 0x1c000
	s_addc_u32 s39, s7, 0
	s_add_u32 s6, s6, 0x1e000
	s_addc_u32 s7, s7, 0
	s_waitcnt vmcnt(6) lgkmcnt(0)
	v_mfma_f32_32x32x16_bf16 v[0:15], v[90:93], v[72:75], v[0:15]
	ds_read_b128 v[86:89], v85
	ds_read_b128 v[90:93], v85 offset:256
	s_waitcnt lgkmcnt(1)
	v_mfma_f32_32x32x16_bf16 v[0:15], v[86:89], v[52:55], v[0:15]
	v_add_u32_e32 v86, v101, v104
	v_add_u32_e32 v87, v101, v105
	s_waitcnt vmcnt(5) lgkmcnt(0)
	v_mfma_f32_32x32x16_bf16 v[0:15], v[90:93], v[64:67], v[0:15]
	ds_read_b128 v[88:91], v86
	ds_read_b128 v[92:95], v86 offset:256
	s_waitcnt lgkmcnt(1)
	v_mfma_f32_32x32x16_bf16 v[0:15], v[88:91], v[48:51], v[0:15]
	s_waitcnt vmcnt(4) lgkmcnt(0)
	v_mfma_f32_32x32x16_bf16 v[0:15], v[92:95], v[56:59], v[0:15]
	ds_read_b128 v[88:91], v87
	ds_read_b128 v[92:95], v87 offset:256
	s_waitcnt lgkmcnt(1)
	v_mfma_f32_32x32x16_bf16 v[0:15], v[88:91], v[36:39], v[0:15]
	v_add_u32_e32 v88, v101, v106
	v_add_u32_e32 v89, v101, v107
	s_waitcnt vmcnt(3) lgkmcnt(0)
	v_mfma_f32_32x32x16_bf16 v[0:15], v[92:95], v[44:47], v[0:15]
	ds_read_b128 v[90:93], v88
	ds_read_b128 v[94:97], v88 offset:256
	s_waitcnt lgkmcnt(1)
	v_mfma_f32_32x32x16_bf16 v[0:15], v[90:93], v[28:31], v[0:15]
	v_xor_b32_e32 v91, 0xc0, v100
	v_add_u32_e32 v90, v101, v91
	v_add_u32_e32 v101, 0x10000, v101
	v_add_u32_e32 v100, v101, v100
	v_add_u32_e32 v91, v101, v91
	s_waitcnt vmcnt(2) lgkmcnt(0)
	v_mfma_f32_32x32x16_bf16 v[0:15], v[94:97], v[40:43], v[0:15]
	ds_read_b128 v[92:95], v90
	ds_read_b128 v[96:99], v90 offset:256
	s_waitcnt lgkmcnt(1)
	v_mfma_f32_32x32x16_bf16 v[0:15], v[92:95], v[24:27], v[0:15]
	ds_read_b128 v[92:95], v89
	s_waitcnt vmcnt(1) lgkmcnt(1)
	v_mfma_f32_32x32x16_bf16 v[0:15], v[96:99], v[32:35], v[0:15]
	ds_read_b128 v[96:99], v89 offset:256
	s_waitcnt lgkmcnt(1)
	v_mfma_f32_32x32x16_bf16 v[0:15], v[92:95], v[20:23], v[0:15]
	s_waitcnt vmcnt(0) lgkmcnt(0)
	v_mfma_f32_32x32x16_bf16 v[0:15], v[96:99], v[16:19], v[0:15]
	s_nop 11
	v_cvt_pk_bf16_f32 v0, v0, v1
	v_cvt_pk_bf16_f32 v1, v2, v3
	v_cvt_pk_bf16_f32 v2, v4, v5
	v_cvt_pk_bf16_f32 v3, v6, v7
	v_cvt_pk_bf16_f32 v4, v8, v9
	v_cvt_pk_bf16_f32 v5, v10, v11
	v_cvt_pk_bf16_f32 v6, v12, v13
	v_cvt_pk_bf16_f32 v7, v14, v15
	ds_write_b128 v82, v[0:3]
	ds_write_b128 v82, v[4:7] offset:1024
	s_waitcnt lgkmcnt(0)
	s_barrier
	s_mov_b32 s5, m0
	s_mov_b32 m0, s21
	s_nop 0
	global_load_lds_dwordx4 v192, s[18:19]
	s_mov_b32 m0, s5
	s_nop 0
	s_mov_b32 s5, m0
	s_mov_b32 m0, s31
	s_nop 0
	global_load_lds_dwordx4 v192, s[36:37]
	s_mov_b32 m0, s5
	s_nop 0
	s_mov_b32 s5, m0
	s_mov_b32 m0, s33
	s_nop 0
	global_load_lds_dwordx4 v192, s[38:39]
	s_mov_b32 m0, s5
	s_nop 0
	s_mov_b32 s5, m0
	s_mov_b32 m0, s34
	s_nop 0
	global_load_lds_dwordx4 v192, s[6:7]
	s_mov_b32 m0, s5
	ds_read_b128 v[0:3], v80 offset:256
	ds_read2_b32 v[4:5], v80 offset0:72 offset1:73
	ds_read_b128 v[92:95], v83 offset:32768
	ds_read2_b32 v[6:7], v80 offset0:74 offset1:75
	ds_read2_b32 v[8:9], v80 offset0:80 offset1:81
	ds_read2_b32 v[10:11], v80 offset0:82 offset1:83
	ds_read2_b32 v[12:13], v80 offset0:88 offset1:89
	ds_read2_b32 v[14:15], v80 offset0:90 offset1:91
	ds_read_b128 v[96:99], v83 offset:33024
	s_waitcnt lgkmcnt(1)
	v_mfma_f32_32x32x16_bf16 v[0:15], v[92:95], v[68:71], v[0:15]
	s_add_u32 s6, s14, 0x2000
	s_addc_u32 s7, s15, 0
	s_add_u32 s18, s14, 0x4000
	s_addc_u32 s19, s15, 0
	s_add_u32 s34, s14, 0x6000
	s_addc_u32 s35, s15, 0
	s_waitcnt lgkmcnt(0)
	v_mfma_f32_32x32x16_bf16 v[0:15], v[96:99], v[76:79], v[0:15]
	ds_read_b128 v[92:95], v84 offset:32768
	ds_read_b128 v[96:99], v84 offset:33024
	s_waitcnt lgkmcnt(1)
	v_mfma_f32_32x32x16_bf16 v[0:15], v[92:95], v[60:63], v[0:15]
	s_waitcnt lgkmcnt(0)
	v_mfma_f32_32x32x16_bf16 v[0:15], v[96:99], v[72:75], v[0:15]
	ds_read_b128 v[92:95], v85 offset:32768
	ds_read_b128 v[96:99], v85 offset:33024
	s_waitcnt lgkmcnt(1)
	v_mfma_f32_32x32x16_bf16 v[0:15], v[92:95], v[52:55], v[0:15]
	s_waitcnt lgkmcnt(0)
	v_mfma_f32_32x32x16_bf16 v[0:15], v[96:99], v[64:67], v[0:15]
	ds_read_b128 v[92:95], v86 offset:32768
	ds_read_b128 v[96:99], v86 offset:33024
	s_waitcnt lgkmcnt(1)
	v_mfma_f32_32x32x16_bf16 v[0:15], v[92:95], v[48:51], v[0:15]
	s_waitcnt lgkmcnt(0)
	v_mfma_f32_32x32x16_bf16 v[0:15], v[96:99], v[56:59], v[0:15]
	ds_read_b128 v[92:95], v87 offset:32768
	ds_read_b128 v[96:99], v87 offset:33024
	s_waitcnt lgkmcnt(1)
	v_mfma_f32_32x32x16_bf16 v[0:15], v[92:95], v[36:39], v[0:15]
	s_waitcnt lgkmcnt(0)
	v_mfma_f32_32x32x16_bf16 v[0:15], v[96:99], v[44:47], v[0:15]
	ds_read_b128 v[92:95], v88 offset:32768
	ds_read_b128 v[96:99], v88 offset:33024
	s_waitcnt lgkmcnt(1)
	v_mfma_f32_32x32x16_bf16 v[0:15], v[92:95], v[28:31], v[0:15]
	s_waitcnt lgkmcnt(0)
	v_mfma_f32_32x32x16_bf16 v[0:15], v[96:99], v[40:43], v[0:15]
	ds_read_b128 v[92:95], v90 offset:32768
	ds_read_b128 v[96:99], v90 offset:33024
	s_waitcnt lgkmcnt(1)
	v_mfma_f32_32x32x16_bf16 v[0:15], v[92:95], v[24:27], v[0:15]
	ds_read_b128 v[92:95], v89 offset:32768
	s_waitcnt lgkmcnt(1)
	v_mfma_f32_32x32x16_bf16 v[0:15], v[96:99], v[32:35], v[0:15]
	ds_read_b128 v[96:99], v89 offset:33024
	ds_read_b128 v[128:131], v81
	ds_read_b128 v[132:135], v81 offset:1024
	ds_read_b128 v[136:139], v81 offset:2048
	ds_read_b128 v[140:143], v81 offset:3072
	s_waitcnt lgkmcnt(5)
	v_mfma_f32_32x32x16_bf16 v[0:15], v[92:95], v[20:23], v[0:15]
	s_waitcnt lgkmcnt(4)
	v_mfma_f32_32x32x16_bf16 v[0:15], v[96:99], v[16:19], v[0:15]
	s_nop 11
	v_cvt_pk_bf16_f32 v0, v0, v1
	v_cvt_pk_bf16_f32 v1, v2, v3
	v_cvt_pk_bf16_f32 v2, v4, v5
	v_cvt_pk_bf16_f32 v3, v6, v7
	v_cvt_pk_bf16_f32 v4, v8, v9
	v_cvt_pk_bf16_f32 v5, v10, v11
	v_cvt_pk_bf16_f32 v6, v12, v13
	v_cvt_pk_bf16_f32 v7, v14, v15
	ds_write_b128 v82, v[0:3] offset:20480
	ds_write_b128 v82, v[4:7] offset:21504
	s_waitcnt vmcnt(4) lgkmcnt(0)
	s_barrier
	s_mov_b32 s5, m0
	s_mov_b32 m0, s23
	s_nop 0
	global_load_lds_dwordx4 v192, s[14:15]
	s_mov_b32 m0, s5
	s_nop 0
	s_mov_b32 s5, m0
	s_mov_b32 m0, s24
	s_nop 0
	global_load_lds_dwordx4 v192, s[6:7]
	s_mov_b32 m0, s5
	s_add_u32 s6, s14, 0xa000
	s_mov_b32 s5, m0
	s_mov_b32 m0, s25
	s_nop 0
	global_load_lds_dwordx4 v192, s[18:19]
	s_mov_b32 m0, s5
	s_addc_u32 s7, s15, 0
	s_mov_b32 s5, m0
	s_mov_b32 m0, s26
	s_nop 0
	global_load_lds_dwordx4 v192, s[34:35]
	s_mov_b32 m0, s5
	ds_read_b128 v[0:3], v80 offset:512
	ds_read2_b32 v[4:5], v80 offset0:136 offset1:137
	ds_read_b128 v[92:95], v100
	ds_read2_b32 v[6:7], v80 offset0:138 offset1:139
	ds_read2_b32 v[8:9], v80 offset0:144 offset1:145
	ds_read2_b32 v[10:11], v80 offset0:146 offset1:147
	ds_read2_b32 v[12:13], v80 offset0:152 offset1:153
	ds_read2_b32 v[14:15], v80 offset0:154 offset1:155
	ds_read_b128 v[96:99], v100 offset:256
	s_waitcnt lgkmcnt(1)
	v_mfma_f32_32x32x16_bf16 v[0:15], v[92:95], v[68:71], v[0:15]
	v_add_u32_e32 v100, v101, v102
	s_add_u32 s18, s14, 0xc000
	s_addc_u32 s19, s15, 0
	s_add_u32 s34, s14, 0xe000
	s_addc_u32 s35, s15, 0
	s_cmpk_gt_u32 s3, 0xff
	s_waitcnt lgkmcnt(0)
	v_mfma_f32_32x32x16_bf16 v[0:15], v[96:99], v[76:79], v[0:15]
	ds_read_b128 v[92:95], v100
	ds_read_b128 v[96:99], v100 offset:256
	v_add_u32_e32 v100, v101, v103
	s_waitcnt lgkmcnt(1)
	v_mfma_f32_32x32x16_bf16 v[0:15], v[92:95], v[60:63], v[0:15]
	s_waitcnt lgkmcnt(0)
	v_mfma_f32_32x32x16_bf16 v[0:15], v[96:99], v[72:75], v[0:15]
	ds_read_b128 v[92:95], v100
	ds_read_b128 v[96:99], v100 offset:256
	v_add_u32_e32 v100, v101, v104
	s_waitcnt lgkmcnt(1)
	v_mfma_f32_32x32x16_bf16 v[0:15], v[92:95], v[52:55], v[0:15]
	s_waitcnt lgkmcnt(0)
	v_mfma_f32_32x32x16_bf16 v[0:15], v[96:99], v[64:67], v[0:15]
	ds_read_b128 v[92:95], v100
	ds_read_b128 v[96:99], v100 offset:256
	v_add_u32_e32 v100, v101, v105
	s_waitcnt lgkmcnt(1)
	v_mfma_f32_32x32x16_bf16 v[0:15], v[92:95], v[48:51], v[0:15]
	s_waitcnt lgkmcnt(0)
	v_mfma_f32_32x32x16_bf16 v[0:15], v[96:99], v[56:59], v[0:15]
	ds_read_b128 v[92:95], v100
	ds_read_b128 v[96:99], v100 offset:256
	v_add_u32_e32 v100, v101, v106
	s_waitcnt lgkmcnt(1)
	v_mfma_f32_32x32x16_bf16 v[0:15], v[92:95], v[36:39], v[0:15]
	s_waitcnt lgkmcnt(0)
	v_mfma_f32_32x32x16_bf16 v[0:15], v[96:99], v[44:47], v[0:15]
	ds_read_b128 v[92:95], v100
	ds_read_b128 v[96:99], v100 offset:256
	s_waitcnt lgkmcnt(1)
	v_mfma_f32_32x32x16_bf16 v[0:15], v[92:95], v[28:31], v[0:15]
	s_waitcnt lgkmcnt(0)
	v_mfma_f32_32x32x16_bf16 v[0:15], v[96:99], v[40:43], v[0:15]
	ds_read_b128 v[92:95], v91
	ds_read_b128 v[96:99], v91 offset:256
	v_add_u32_e32 v91, v101, v107
	s_waitcnt lgkmcnt(1)
	v_mfma_f32_32x32x16_bf16 v[0:15], v[92:95], v[24:27], v[0:15]
	ds_read_b128 v[92:95], v91
	s_waitcnt lgkmcnt(1)
	v_mfma_f32_32x32x16_bf16 v[0:15], v[96:99], v[32:35], v[0:15]
	ds_read_b128 v[96:99], v91 offset:256
	ds_read_b128 v[144:147], v81 offset:20480
	ds_read_b128 v[148:151], v81 offset:21504
	ds_read_b128 v[152:155], v81 offset:22528
	ds_read_b128 v[156:159], v81 offset:23552
	s_waitcnt lgkmcnt(5)
	v_mfma_f32_32x32x16_bf16 v[0:15], v[92:95], v[20:23], v[0:15]
	s_waitcnt lgkmcnt(4)
	v_mfma_f32_32x32x16_bf16 v[0:15], v[96:99], v[16:19], v[0:15]
	s_nop 11
	v_cvt_pk_bf16_f32 v0, v0, v1
	v_cvt_pk_bf16_f32 v1, v2, v3
	v_cvt_pk_bf16_f32 v2, v4, v5
	v_cvt_pk_bf16_f32 v3, v6, v7
	v_cvt_pk_bf16_f32 v4, v8, v9
	v_cvt_pk_bf16_f32 v5, v10, v11
	v_cvt_pk_bf16_f32 v6, v12, v13
	v_cvt_pk_bf16_f32 v7, v14, v15
	ds_write_b128 v82, v[0:3]
	ds_write_b128 v82, v[4:7] offset:1024
	s_waitcnt vmcnt(4) lgkmcnt(0)
	s_barrier
	s_mov_b32 s5, m0
	s_mov_b32 m0, s27
	s_nop 0
	global_load_lds_dwordx4 v192, s[16:17]
	s_mov_b32 m0, s5
	s_nop 0
	s_mov_b32 s5, m0
	s_mov_b32 m0, s28
	s_nop 0
	global_load_lds_dwordx4 v192, s[6:7]
	s_mov_b32 m0, s5
	s_movk_i32 s7, 0x80
	s_mov_b32 s5, m0
	s_mov_b32 m0, s29
	s_nop 0
	global_load_lds_dwordx4 v192, s[18:19]
	s_mov_b32 m0, s5
	s_movk_i32 s6, 0xc0
	s_mov_b32 s5, m0
	s_mov_b32 m0, s30
	s_nop 0
	global_load_lds_dwordx4 v192, s[34:35]
	s_mov_b32 m0, s5
	ds_read_b128 v[0:3], v80 offset:768
	ds_read2_b32 v[4:5], v80 offset0:200 offset1:201
	ds_read_b128 v[92:95], v83
	ds_read2_b32 v[6:7], v80 offset0:202 offset1:203
	ds_read2_b32 v[8:9], v80 offset0:208 offset1:209
	ds_read2_b32 v[10:11], v80 offset0:210 offset1:211
	ds_read2_b32 v[12:13], v80 offset0:216 offset1:217
	ds_read2_b32 v[14:15], v80 offset0:218 offset1:219
	ds_read_b128 v[96:99], v83 offset:256
	s_waitcnt lgkmcnt(1)
	v_mfma_f32_32x32x16_bf16 v[0:15], v[92:95], v[68:71], v[0:15]
	s_mov_b32 s5, 0x10000
	s_waitcnt lgkmcnt(0)
	v_mfma_f32_32x32x16_bf16 v[0:15], v[96:99], v[76:79], v[0:15]
	ds_read_b128 v[68:71], v84
	ds_read_b128 v[76:79], v84 offset:256
	s_waitcnt lgkmcnt(1)
	v_mfma_f32_32x32x16_bf16 v[0:15], v[68:71], v[60:63], v[0:15]
	ds_read_b128 v[60:63], v85
	ds_read_b128 v[68:71], v85 offset:256
	s_waitcnt lgkmcnt(2)
	v_mfma_f32_32x32x16_bf16 v[0:15], v[76:79], v[72:75], v[0:15]
	s_waitcnt lgkmcnt(1)
	v_mfma_f32_32x32x16_bf16 v[0:15], v[60:63], v[52:55], v[0:15]
	ds_read_b128 v[52:55], v86
	ds_read_b128 v[60:63], v86 offset:256
	s_waitcnt lgkmcnt(2)
	v_mfma_f32_32x32x16_bf16 v[0:15], v[68:71], v[64:67], v[0:15]
	s_waitcnt lgkmcnt(1)
	v_mfma_f32_32x32x16_bf16 v[0:15], v[52:55], v[48:51], v[0:15]
	ds_read_b128 v[48:51], v87
	ds_read_b128 v[52:55], v87 offset:256
	s_waitcnt lgkmcnt(2)
	v_mfma_f32_32x32x16_bf16 v[0:15], v[60:63], v[56:59], v[0:15]
	s_waitcnt lgkmcnt(1)
	v_mfma_f32_32x32x16_bf16 v[0:15], v[48:51], v[36:39], v[0:15]
	s_waitcnt lgkmcnt(0)
	v_mfma_f32_32x32x16_bf16 v[0:15], v[52:55], v[44:47], v[0:15]
	ds_read_b128 v[36:39], v88
	ds_read_b128 v[44:47], v88 offset:256
	s_waitcnt lgkmcnt(1)
	v_mfma_f32_32x32x16_bf16 v[0:15], v[36:39], v[28:31], v[0:15]
	ds_read_b128 v[28:31], v90
	ds_read_b128 v[36:39], v90 offset:256
	s_waitcnt lgkmcnt(2)
	v_mfma_f32_32x32x16_bf16 v[0:15], v[44:47], v[40:43], v[0:15]
	s_waitcnt lgkmcnt(1)
	v_mfma_f32_32x32x16_bf16 v[0:15], v[28:31], v[24:27], v[0:15]
	ds_read_b128 v[24:27], v89
	ds_read_b128 v[28:31], v89 offset:256
	ds_read_b128 v[160:163], v81
	ds_read_b128 v[164:167], v81 offset:1024
	ds_read_b128 v[168:171], v81 offset:2048
	ds_read_b128 v[172:175], v81 offset:3072
	s_waitcnt lgkmcnt(6)
	v_mfma_f32_32x32x16_bf16 v[0:15], v[36:39], v[32:35], v[0:15]
	s_waitcnt lgkmcnt(5)
	v_mfma_f32_32x32x16_bf16 v[0:15], v[24:27], v[20:23], v[0:15]
	v_mbcnt_lo_u32_b32 v20, -1, 0
	v_mbcnt_hi_u32_b32 v193, -1, v20
	v_mov_b32_e32 v194, v193
	s_waitcnt lgkmcnt(4)
	v_mfma_f32_32x32x16_bf16 v[0:15], v[28:31], v[16:19], v[0:15]
	s_nop 11
	v_cvt_pk_bf16_f32 v0, v0, v1
	v_cvt_pk_bf16_f32 v1, v2, v3
	v_cvt_pk_bf16_f32 v2, v4, v5
	v_cvt_pk_bf16_f32 v3, v6, v7
	v_cvt_pk_bf16_f32 v4, v8, v9
	v_cvt_pk_bf16_f32 v5, v10, v11
	v_cvt_pk_bf16_f32 v6, v12, v13
	v_cvt_pk_bf16_f32 v7, v14, v15
	ds_write_b128 v82, v[0:3] offset:20480
	ds_write_b128 v82, v[4:7] offset:21504
	s_waitcnt vmcnt(4) lgkmcnt(0)
	s_barrier
	ds_read_b128 v[176:179], v81 offset:20480
	ds_read_b128 v[180:183], v81 offset:21504
	ds_read_b128 v[184:187], v81 offset:22528
	ds_read_b128 v[188:191], v81 offset:23552
	s_waitcnt lgkmcnt(0)
	s_barrier
	s_nop 0
	v_and_b32_e32 v196, 31, v194
	v_ashrrev_i32_e32 v197, 5, v194
	v_lshlrev_b32_e32 v195, 2, v194
	v_bfe_u32 v198, v194, 2, 2
	s_cbranch_scc0 .LBB1_16
	v_lshl_add_u32 v0, s20, 2, v197
	v_lshlrev_b32_e32 v3, 2, v197
	v_add_u32_e32 v1, 2, v0
	v_lshlrev_b32_e32 v2, 9, v0
	v_and_b32_e32 v3, 12, v3
	v_bfe_u32 v0, v0, 2, 2
	v_bitop3_b32 v0, v0, v196, v3 bitop3:0x36
	v_lshl_or_b32 v199, v0, 4, v2
	v_lshlrev_b32_e32 v0, 2, v1
	s_bfe_u32 s18, s3, 0x10006
	v_and_b32_e32 v0, 12, v0
	v_bfe_u32 v2, v1, 2, 2
	v_bitop3_b32 v0, v0, v196, v2 bitop3:0x36
	v_lshrrev_b32_e32 v2, 3, v194
	s_lshl_b32 s16, s18, 8
	v_and_b32_e32 v2, 2, v2
	v_bfe_u32 v3, v194, 1, 1
	s_add_i32 s16, s16, 0
	v_lshlrev_b32_e32 v4, 3, v194
	v_lshl_add_u32 v5, v197, 11, s16
	v_bitop3_b32 v2, v2, v197, v3 bitop3:0x36
	v_and_or_b32 v4, v4, 8, v5
	v_lshlrev_b32_e32 v2, 4, v2
	v_lshlrev_b32_e32 v3, 6, v198
	v_lshl_add_u32 v4, v198, 9, v4
	v_or_b32_e32 v5, v2, v3
	v_add_u32_e32 v200, v4, v5
	v_bitop3_b32 v5, v2, v3, 32 bitop3:0xde
	v_add_u32_e32 v6, 0x1000, v4
	v_add_u32_e32 v201, v6, v5
	v_xor_b32_e32 v5, 64, v3
	v_bitop3_b32 v5, v2, v5, 32 bitop3:0xde
	v_add_u32_e32 v203, v6, v5
	v_xor_b32_e32 v5, 0x80, v3
	v_bitop3_b32 v7, v2, v3, 64 bitop3:0xf6
	v_bitop3_b32 v5, v2, v5, 32 bitop3:0xde
	v_add_u32_e32 v202, v4, v7
	v_bitop3_b32 v7, v2, v3, s7 bitop3:0xf6
	v_add_u32_e32 v205, v6, v5
	v_xor_b32_e32 v5, 0xc0, v3
	v_bitop3_b32 v3, v2, v3, s6 bitop3:0xf6
	s_and_b32 s6, s22, 2
	v_lshlrev_b32_e32 v1, 9, v1
	s_lshl_b32 s27, s6, 2
	s_lshl_b32 s7, s6, 8
	s_lshl_b32 s6, s6, 12
	v_lshl_or_b32 v208, v0, 4, v1
	s_lshl_b32 s19, s20, 11
	s_add_i32 s7, s7, 0
	s_add_i32 s6, s6, 0
	v_mov_b32_e32 v0, 0
	v_bitop3_b32 v2, v2, v5, 32 bitop3:0xde
	s_waitcnt vmcnt(0)
	s_add_i32 s19, s19, 0
	s_add_i32 s16, s7, 0x20000
	s_add_i32 s7, s7, 0x20100
	v_lshlrev_b32_e32 v209, 4, v194
	s_add_i32 s6, s6, 0x18000
	v_mov_b32_e32 v14, v0
	v_mov_b32_e32 v15, v0
	v_add_u32_e32 v204, v4, v7
	v_add_u32_e32 v206, v4, v3
	v_add_u32_e32 v207, v6, v2
	v_add_u32_e32 v212, s6, v209
	s_add_u32 s6, s8, 0xfff90000
	v_mov_b32_e32 v1, v0
	v_mov_b32_e32 v2, v0
	v_mov_b32_e32 v3, v0
	v_mov_b32_e32 v4, v0
	v_mov_b32_e32 v5, v0
	v_mov_b32_e32 v6, v0
	v_mov_b32_e32 v7, v0
	v_mov_b32_e32 v8, v0
	v_mov_b32_e32 v9, v0
	v_mov_b32_e32 v10, v0
	v_mov_b32_e32 v11, v0
	v_mov_b32_e32 v12, v0
	v_mov_b32_e32 v13, v0
	v_mov_b64_e32 v[62:63], v[14:15]
	v_mov_b64_e32 v[94:95], v[14:15]
	v_mov_b64_e32 v[126:127], v[14:15]
	v_mov_b64_e32 v[30:31], v[14:15]
	v_mov_b64_e32 v[46:47], v[14:15]
	v_mov_b64_e32 v[78:79], v[14:15]
	v_mov_b64_e32 v[110:111], v[14:15]
	v_add_u32_e32 v210, s16, v195
	v_add_u32_e32 v211, s7, v195
	s_addc_u32 s7, s9, -1
	s_mov_b32 s33, 1
	s_mov_b32 s31, 0x8000
	s_mov_b32 s29, 0x10000
	v_mov_b64_e32 v[60:61], v[12:13]
	v_mov_b64_e32 v[58:59], v[10:11]
	v_mov_b64_e32 v[56:57], v[8:9]
	v_mov_b64_e32 v[54:55], v[6:7]
	v_mov_b64_e32 v[52:53], v[4:5]
	v_mov_b64_e32 v[50:51], v[2:3]
	v_mov_b64_e32 v[48:49], v[0:1]
	v_mov_b64_e32 v[92:93], v[12:13]
	v_mov_b64_e32 v[90:91], v[10:11]
	v_mov_b64_e32 v[88:89], v[8:9]
	v_mov_b64_e32 v[86:87], v[6:7]
	v_mov_b64_e32 v[84:85], v[4:5]
	v_mov_b64_e32 v[82:83], v[2:3]
	v_mov_b64_e32 v[80:81], v[0:1]
	v_mov_b64_e32 v[124:125], v[12:13]
	v_mov_b64_e32 v[122:123], v[10:11]
	v_mov_b64_e32 v[120:121], v[8:9]
	v_mov_b64_e32 v[118:119], v[6:7]
	v_mov_b64_e32 v[116:117], v[4:5]
	v_mov_b64_e32 v[114:115], v[2:3]
	v_mov_b64_e32 v[112:113], v[0:1]
	v_mov_b64_e32 v[28:29], v[12:13]
	v_mov_b64_e32 v[26:27], v[10:11]
	v_mov_b64_e32 v[24:25], v[8:9]
	v_mov_b64_e32 v[22:23], v[6:7]
	v_mov_b64_e32 v[20:21], v[4:5]
	v_mov_b64_e32 v[18:19], v[2:3]
	v_mov_b64_e32 v[16:17], v[0:1]
	v_mov_b64_e32 v[44:45], v[12:13]
	v_mov_b64_e32 v[42:43], v[10:11]
	v_mov_b64_e32 v[40:41], v[8:9]
	v_mov_b64_e32 v[38:39], v[6:7]
	v_mov_b64_e32 v[36:37], v[4:5]
	v_mov_b64_e32 v[34:35], v[2:3]
	v_mov_b64_e32 v[32:33], v[0:1]
	v_mov_b64_e32 v[76:77], v[12:13]
	v_mov_b64_e32 v[74:75], v[10:11]
	v_mov_b64_e32 v[72:73], v[8:9]
	v_mov_b64_e32 v[70:71], v[6:7]
	v_mov_b64_e32 v[68:69], v[4:5]
	v_mov_b64_e32 v[66:67], v[2:3]
	v_mov_b64_e32 v[64:65], v[0:1]
	v_mov_b64_e32 v[108:109], v[12:13]
	v_mov_b64_e32 v[106:107], v[10:11]
	v_mov_b64_e32 v[104:105], v[8:9]
	v_mov_b64_e32 v[102:103], v[6:7]
	v_mov_b64_e32 v[100:101], v[4:5]
	v_mov_b64_e32 v[98:99], v[2:3]
	v_mov_b64_e32 v[96:97], v[0:1]
	s_waitcnt lgkmcnt(0)
	s_barrier

	.amdhsa_kernel _Z12fused_kernelPKtS0_PKfS0_S2_S2_Pf
		.amdhsa_group_segment_fixed_size 0
		.amdhsa_private_segment_fixed_size 0
		.amdhsa_kernarg_size 56
		.amdhsa_user_sgpr_count 2
		.amdhsa_user_sgpr_dispatch_ptr 0
		.amdhsa_user_sgpr_queue_ptr 0
		.amdhsa_user_sgpr_kernarg_segment_ptr 1
		.amdhsa_user_sgpr_dispatch_id 0
		.amdhsa_user_sgpr_kernarg_preload_length 0
		.amdhsa_user_sgpr_kernarg_preload_offset 0
		.amdhsa_user_sgpr_private_segment_size 0
		.amdhsa_uses_dynamic_stack 0
		.amdhsa_enable_private_segment 0
		.amdhsa_system_sgpr_workgroup_id_x 1
		.amdhsa_system_sgpr_workgroup_id_y 0
		.amdhsa_system_sgpr_workgroup_id_z 0
		.amdhsa_system_sgpr_workgroup_info 0
		.amdhsa_system_vgpr_workitem_id 0
		.amdhsa_next_free_vgpr 246
		.amdhsa_next_free_sgpr 44
		.amdhsa_accum_offset 248
		.amdhsa_reserve_vcc 1
		.amdhsa_float_round_mode_32 0
		.amdhsa_float_round_mode_16_64 0
		.amdhsa_float_denorm_mode_32 3
		.amdhsa_float_denorm_mode_16_64 3
		.amdhsa_dx10_clamp 1
		.amdhsa_ieee_mode 1
		.amdhsa_fp16_overflow 0
		.amdhsa_tg_split 0
		.amdhsa_exception_fp_ieee_invalid_op 0
		.amdhsa_exception_fp_denorm_src 0
		.amdhsa_exception_fp_ieee_div_zero 0
		.amdhsa_exception_fp_ieee_overflow 0
		.amdhsa_exception_fp_ieee_underflow 0
		.amdhsa_exception_fp_ieee_inexact 0
		.amdhsa_exception_int_div_zero 0
	.end_amdhsa_kernel

amdhsa.kernels:
  - .agpr_count:     0
    .args:
      - .actual_access:  read_only
        .address_space:  global
        .offset:         0
        .size:           8
        .value_kind:     global_buffer
      - .actual_access:  read_only
        .address_space:  global
        .offset:         8
        .size:           8
        .value_kind:     global_buffer
      - .actual_access:  read_only
        .address_space:  global
        .offset:         16
        .size:           8
        .value_kind:     global_buffer
      - .actual_access:  read_only
        .address_space:  global
        .offset:         24
        .size:           8
        .value_kind:     global_buffer
      - .actual_access:  read_only
        .address_space:  global
        .offset:         32
        .size:           8
        .value_kind:     global_buffer
      - .address_space:  global
        .offset:         40
        .size:           8
        .value_kind:     global_buffer
      - .actual_access:  write_only
        .address_space:  global
        .offset:         48
        .size:           8
        .value_kind:     global_buffer
      - .actual_access:  write_only
        .address_space:  global
        .offset:         56
        .size:           8
        .value_kind:     global_buffer
      - .actual_access:  write_only
        .address_space:  global
        .offset:         64
        .size:           8
        .value_kind:     global_buffer
    .group_segment_fixed_size: 21520
    .kernarg_segment_align: 8
    .kernarg_segment_size: 72
    .language:       OpenCL C
    .language_version:
      - 2
      - 0
    .max_flat_workgroup_size: 256
    .name:           _Z11prep_kernelPKfS0_S0_S0_S0_PtS1_PfS1_
    .private_segment_fixed_size: 0
    .sgpr_count:     20
    .sgpr_spill_count: 0
    .symbol:         _Z11prep_kernelPKfS0_S0_S0_S0_PtS1_PfS1_.kd
    .uniform_work_group_size: 1
    .uses_dynamic_stack: false
    .vgpr_count:     70
    .vgpr_spill_count: 0
    .wavefront_size: 64
  - .agpr_count:     0
    .args:
      - .address_space:  global
        .offset:         0
        .size:           8
        .value_kind:     global_buffer
      - .address_space:  global
        .offset:         8
        .size:           8
        .value_kind:     global_buffer
      - .actual_access:  read_only
        .address_space:  global
        .offset:         16
        .size:           8
        .value_kind:     global_buffer
      - .address_space:  global
        .offset:         24
        .size:           8
        .value_kind:     global_buffer
      - .actual_access:  read_only
        .address_space:  global
        .offset:         32
        .size:           8
        .value_kind:     global_buffer
      - .actual_access:  read_only
        .address_space:  global
        .offset:         40
        .size:           8
        .value_kind:     global_buffer
      - .actual_access:  write_only
        .address_space:  global
        .offset:         48
        .size:           8
        .value_kind:     global_buffer
    .group_segment_fixed_size: 0
    .kernarg_segment_align: 8
    .kernarg_segment_size: 56
    .language:       OpenCL C
    .language_version:
      - 2
      - 0
    .max_flat_workgroup_size: 512
    .name:           _Z12fused_kernelPKtS0_PKfS0_S2_S2_Pf
    .private_segment_fixed_size: 0
    .sgpr_count:     50
    .sgpr_spill_count: 0
    .symbol:         _Z12fused_kernelPKtS0_PKfS0_S2_S2_Pf.kd
    .uniform_work_group_size: 1
    .uses_dynamic_stack: false
    .vgpr_count:     246
    .vgpr_spill_count: 0
    .wavefront_size: 64
